# worker GCN1 GEMM: direct ReLU without canonicalising v_max chain (8 fewer instrs per tile)
# speedup vs baseline: 1.0043x; 1.0037x over previous
.LBB1_361:
	v_add_u32_e32 v42, s2, v28
	v_ashrrev_i32_e32 v43, 31, v42
	v_lshl_add_u64 v[38:39], v[42:43], 2, s[50:51]
	global_load_dword v44, v[38:39], off
	v_subrev_u32_e32 v29, 64, v1
	ds_read_b128 v[30:33], v29
	ds_read_b128 v[38:41], v1
	s_waitcnt vmcnt(2) lgkmcnt(1)
	v_mfma_f32_16x16x32_f16 v[34:37], v[2:5], v[30:33], v[18:21]
	s_add_i32 s2, s2, 16
	v_lshlrev_b64 v[42:43], 8, v[42:43]
	v_add_u32_e32 v1, 0x900, v1
	s_waitcnt vmcnt(1)
	v_mfma_f32_16x16x32_f16 v[30:33], v[10:13], v[30:33], v[22:25]
	s_cmpk_lg_i32 s2, 0x50
	v_lshl_add_u64 v[42:43], v[26:27], 0, v[42:43]
	s_waitcnt lgkmcnt(0)
	v_mfma_f32_16x16x32_f16 v[34:37], v[6:9], v[38:41], v[34:37]
	v_mfma_f32_16x16x32_f16 v[30:33], v[14:17], v[38:41], v[30:33]
	s_nop 6
	v_max_f32_e32 v29, 0, v34
	v_max_f32_e32 v34, 0, v37
	v_max_f32_e32 v37, 0, v30
	v_max_f32_e32 v30, 0, v35
	v_max_f32_e32 v38, 0, v31
	v_max_f32_e32 v31, 0, v36
	v_max_f32_e32 v39, 0, v32
	v_max_f32_e32 v40, 0, v33
	s_waitcnt vmcnt(0)
	v_pk_mul_f32 v[30:31], v[44:45], v[30:31] op_sel_hi:[0,1]
	v_fma_mixlo_f16 v29, v44, v29, 0
	v_fma_mixlo_f16 v34, v44, v34, 0
	v_pk_mul_f32 v[32:33], v[44:45], v[38:39] op_sel_hi:[0,1]
	v_cvt_pk_f16_f32 v31, v30, v31
	v_fma_mixlo_f16 v35, v44, v37, 0
	v_fma_mixlo_f16 v36, v44, v40, 0
	v_cvt_pk_f16_f32 v33, v32, v33
	v_pack_b32_f16 v30, v29, v31
	v_alignbit_b32 v31, v34, v31, 16
	v_pack_b32_f16 v32, v35, v33
	v_alignbit_b32 v33, v36, v33, 16
	global_store_dwordx2 v[42:43], v[30:31], off
	global_store_dwordx2 v[42:43], v[32:33], off offset:32
	s_cbranch_scc1 .LBB1_361
	s_setprio 0
	s_setprio 0
